# P5 EpiSwiglu epilogue rewritten by hand with packed f32 math (v_pk_mul/fma/add), n-major order, + P7 LN gamma/beta hoist + barrier-0 census parallel loads
# speedup vs baseline: 1.0102x; 1.0102x over previous
; #define PG8_LAS __attribute__((address_space(3)))
;     __device__ __forceinline__ void operator()(const i32x4 (&acc)[2][2][4][2], const Unit& u, int wr, int wc, int fr, int fq, PG8_LAS unsigned* scr) const {
;         const int j = u.pn & 7;
;         const int row0 = u.pm * BM + wr * 64 + fr, c0 = j * 128 + wc * 32 + 8 * fq, cl = wc * 32 + 8 * fq;
;         f32x4 bgv[2], buv[2], csg[2], csu[2];
;         constexpr float C2 = 1.702f * 1.44269504f;
; #pragma unroll
;         for (int n = 0; n < 2; ++n) { bgv[n] = *(const PG8_LAS f32x4*)(scr + 512 + cl + 4 * n) * C2; buv[n] = *(const PG8_LAS f32x4*)(scr + 512 + 128 + cl + 4 * n);
;             csg[n] = *(const PG8_LAS f32x4*)(scr + 256 + cl + 4 * n) * (C2 / 127.0f); csu[n] = *(const PG8_LAS f32x4*)(scr + 256 + 128 + cl + 4 * n) * (1.0f / 127.0f); }
; #pragma unroll
;         for (int ai = 0; ai < 2; ++ai)
; #pragma unroll
;             for (int mp = 0; mp < 4; mp += 2) { unsigned wp[2][2];
; #pragma unroll
;                 for (int hm = 0; hm < 2; ++hm) { const int m = mp + hm; const int r = ai * HALF + wr * 64 + m * 16 + fr; const float rs = __uint_as_float(scr[r]); float o[8];
; #pragma unroll
;                     for (int n = 0; n < 2; ++n) { const f32x4 sgr = csg[n] * rs, sur = csu[n] * rs;
; #pragma unroll
;                         for (int q = 0; q < 4; ++q) { const float h = fminf(__builtin_fmaf((float)acc[ai][0][m][n][q], sgr[q], bgv[n][q]), 7.0f * C2), up = fminf(fmaxf(__builtin_fmaf((float)acc[ai][1][m][n][q], sur[q], buv[n][q]), -7.0f), 7.0f);
;                             const float sg = __builtin_amdgcn_rcpf(1.0f + __builtin_amdgcn_exp2f(-h)); o[4 * n + q] = __builtin_fmaf(up, ACT_SC / C2, ACT_SC / C2) * (h * sg); } }
;                     int w0 = __builtin_amdgcn_cvt_pk_fp8_f32(o[0], o[1], 0, false); w0 = __builtin_amdgcn_cvt_pk_fp8_f32(o[2], o[3], w0, true);
;                     int w1 = __builtin_amdgcn_cvt_pk_fp8_f32(o[4], o[5], 0, false); w1 = __builtin_amdgcn_cvt_pk_fp8_f32(o[6], o[7], w1, true);
;                     wp[hm][0] = (unsigned)w0; wp[hm][1] = (unsigned)w1; }
.LBB0_807:
	s_waitcnt vmcnt(32)
	ds_write_b32 v182, v205
	s_and_saveexec_b64 s[10:11], s[34:35]
	ds_write_b32 v182, v204 offset:2048
	s_or_b64 exec, exec, s[10:11]
	v_mov_b32_e32 v162, v168
	s_waitcnt lgkmcnt(0)
	s_barrier
	v_ashrrev_i32_e32 v185, 2, v168
	v_and_b32_e32 v185, 0xffffffc0, v185
	v_bfe_u32 v201, v168, 4, 2
	v_lshrrev_b32_e32 v208, 1, v168
	v_and_b32_e32 v208, 0x60, v208
	v_lshl_or_b32 v208, v201, 3, v208
	s_lshl_b32 s10, s39, 7
	s_and_b32 s10, s10, 0x380
	v_and_b32_e32 v201, 1, v201
	v_lshlrev_b32_e32 v207, 3, v201
	v_add_u32_e32 v206, s10, v208
	v_sub_u32_e32 v206, v206, v207
	v_mov_b32_e32 v207, 0
	v_lshlrev_b32_e32 v201, 4, v201
	v_lshlrev_b32_e32 v208, 2, v208
	v_readlane_b32 s10, v255, 5
	v_and_b32_e32 v160, 15, v168
	v_lshl_add_u32 v161, v185, 2, 0
	v_lshl_add_u32 v161, v160, 2, v161
	v_add_u32_e32 v161, s10, v161
	ds_read2_b32 v[152:153], v161 offset0:0 offset1:16
	ds_read2_b32 v[154:155], v161 offset0:32 offset1:48
	ds_read2_b32 v[156:157], v161 offset0:128 offset1:144
	ds_read2_b32 v[158:159], v161 offset0:160 offset1:176
	v_lshl_add_u32 v185, s40, 8, v185
	v_or_b32_e32 v185, v185, v160
	v_add_u32_e32 v185, v185, v201
	s_mov_b32 s100, 0x405083aa
	s_mov_b32 s101, 0x405083aa
	v_add_u32_e32 v160, 0x21100, v208
	ds_read_b128 v[136:139], v160
	v_add_u32_e32 v160, 0x21300, v208
	ds_read_b128 v[140:143], v160
	v_add_u32_e32 v160, 0x20d00, v208
	ds_read_b128 v[144:147], v160
	v_add_u32_e32 v160, 0x20f00, v208
	ds_read_b128 v[148:151], v160
	s_waitcnt lgkmcnt(0)
	v_mul_f32_e32 v136, 0x401d265f, v136
	v_mul_f32_e32 v137, 0x401d265f, v137
	v_mul_f32_e32 v138, 0x401d265f, v138
	v_mul_f32_e32 v139, 0x401d265f, v139
	v_mul_f32_e32 v144, 0x3c9e6325, v144
	v_mul_f32_e32 v145, 0x3c9e6325, v145
	v_mul_f32_e32 v146, 0x3c9e6325, v146
	v_mul_f32_e32 v147, 0x3c9e6325, v147
	v_mul_f32_e32 v148, 0x3c010204, v148
	v_mul_f32_e32 v149, 0x3c010204, v149
	v_mul_f32_e32 v150, 0x3c010204, v150
	v_mul_f32_e32 v151, 0x3c010204, v151
	v_cvt_f32_i32_e32 v128, v128
	v_cvt_f32_i32_e32 v129, v129
	v_cvt_f32_i32_e32 v130, v130
	v_cvt_f32_i32_e32 v131, v131
	v_cvt_f32_i32_e32 v132, v132
	v_cvt_f32_i32_e32 v133, v133
	v_cvt_f32_i32_e32 v134, v134
	v_cvt_f32_i32_e32 v135, v135
	v_pk_mul_f32 v[160:161], v[144:145], v[152:153] op_sel_hi:[1,0]
	v_pk_mul_f32 v[162:163], v[146:147], v[152:153] op_sel_hi:[1,0]
	v_pk_fma_f32 v[128:129], v[128:129], v[160:161], v[136:137]
	v_pk_fma_f32 v[130:131], v[130:131], v[162:163], v[138:139]
	v_pk_mul_f32 v[160:161], v[148:149], v[152:153] op_sel_hi:[1,0]
	v_pk_mul_f32 v[162:163], v[150:151], v[152:153] op_sel_hi:[1,0]
	v_min_f32_e32 v128, 0x41898193, v128
	v_min_f32_e32 v129, 0x41898193, v129
	v_min_f32_e32 v130, 0x41898193, v130
	v_min_f32_e32 v131, 0x41898193, v131
	v_pk_fma_f32 v[132:133], v[132:133], v[160:161], v[140:141]
	v_pk_fma_f32 v[134:135], v[134:135], v[162:163], v[142:143]
	v_exp_f32_e64 v160, -v128
	v_exp_f32_e64 v161, -v129
	v_exp_f32_e64 v162, -v130
	v_exp_f32_e64 v163, -v131
	v_med3_f32 v132, v132, s8, v199
	v_med3_f32 v133, v133, s8, v199
	v_med3_f32 v134, v134, s8, v199
	v_med3_f32 v135, v135, s8, v199
	v_pk_add_f32 v[160:161], v[160:161], 1.0 op_sel_hi:[1,0]
	v_pk_add_f32 v[162:163], v[162:163], 1.0 op_sel_hi:[1,0]
	v_pk_fma_f32 v[132:133], v[132:133], s[100:101], s[100:101]
	v_pk_fma_f32 v[134:135], v[134:135], s[100:101], s[100:101]
	v_rcp_f32_e32 v160, v160
	v_rcp_f32_e32 v161, v161
	v_rcp_f32_e32 v162, v162
	v_rcp_f32_e32 v163, v163
	v_nop
	v_pk_mul_f32 v[128:129], v[128:129], v[160:161]
	v_pk_mul_f32 v[130:131], v[130:131], v[162:163]
	v_pk_mul_f32 v[128:129], v[132:133], v[128:129]
	v_pk_mul_f32 v[130:131], v[134:135], v[130:131]
	v_cvt_pk_fp8_f32 v128, v128, v129
	v_cvt_pk_fp8_f32 v128, v130, v131 op_sel:[0,0,1]
	v_cvt_f32_i32_e32 v112, v112
	v_cvt_f32_i32_e32 v113, v113
	v_cvt_f32_i32_e32 v114, v114
	v_cvt_f32_i32_e32 v115, v115
	v_cvt_f32_i32_e32 v116, v116
	v_cvt_f32_i32_e32 v117, v117
	v_cvt_f32_i32_e32 v118, v118
	v_cvt_f32_i32_e32 v119, v119
	v_pk_mul_f32 v[202:203], v[144:145], v[152:153] op_sel:[0,1] op_sel_hi:[1,1]
	v_pk_mul_f32 v[204:205], v[146:147], v[152:153] op_sel:[0,1] op_sel_hi:[1,1]
	v_pk_fma_f32 v[112:113], v[112:113], v[202:203], v[136:137]
	v_pk_fma_f32 v[114:115], v[114:115], v[204:205], v[138:139]
	v_pk_mul_f32 v[202:203], v[148:149], v[152:153] op_sel:[0,1] op_sel_hi:[1,1]
	v_pk_mul_f32 v[204:205], v[150:151], v[152:153] op_sel:[0,1] op_sel_hi:[1,1]
	v_min_f32_e32 v112, 0x41898193, v112
	v_min_f32_e32 v113, 0x41898193, v113
	v_min_f32_e32 v114, 0x41898193, v114
	v_min_f32_e32 v115, 0x41898193, v115
	v_pk_fma_f32 v[116:117], v[116:117], v[202:203], v[140:141]
	v_pk_fma_f32 v[118:119], v[118:119], v[204:205], v[142:143]
	v_exp_f32_e64 v202, -v112
	v_exp_f32_e64 v203, -v113
	v_exp_f32_e64 v204, -v114
	v_exp_f32_e64 v205, -v115
	v_med3_f32 v116, v116, s8, v199
	v_med3_f32 v117, v117, s8, v199
	v_med3_f32 v118, v118, s8, v199
	v_med3_f32 v119, v119, s8, v199
	v_pk_add_f32 v[202:203], v[202:203], 1.0 op_sel_hi:[1,0]
	v_pk_add_f32 v[204:205], v[204:205], 1.0 op_sel_hi:[1,0]
	v_pk_fma_f32 v[116:117], v[116:117], s[100:101], s[100:101]
	v_pk_fma_f32 v[118:119], v[118:119], s[100:101], s[100:101]
	v_rcp_f32_e32 v202, v202
	v_rcp_f32_e32 v203, v203
	v_rcp_f32_e32 v204, v204
	v_rcp_f32_e32 v205, v205
	v_nop
	v_pk_mul_f32 v[112:113], v[112:113], v[202:203]
	v_pk_mul_f32 v[114:115], v[114:115], v[204:205]
	v_pk_mul_f32 v[112:113], v[116:117], v[112:113]
	v_pk_mul_f32 v[114:115], v[118:119], v[114:115]
	v_cvt_pk_fp8_f32 v130, v112, v113
	v_cvt_pk_fp8_f32 v130, v114, v115 op_sel:[0,0,1]
	v_cvt_f32_i32_e32 v96, v96
	v_cvt_f32_i32_e32 v97, v97
	v_cvt_f32_i32_e32 v98, v98
	v_cvt_f32_i32_e32 v99, v99
;     __device__ __forceinline__ void operator()(const i32x4 (&acc)[2][2][4][2], const Unit& u, int wr, int wc, int fr, int fq, PG8_LAS unsigned* scr) const {
;     ...
;                 for (int hm = 0; hm < 2; ++hm) { const int m = mp + hm; const int r = ai * HALF + wr * 64 + m * 16 + fr; const float rs = __uint_as_float(scr[r]); float o[8];
; #pragma unroll
;                     for (int n = 0; n < 2; ++n) { const f32x4 sgr = csg[n] * rs, sur = csu[n] * rs;
; #pragma unroll
;                         for (int q = 0; q < 4; ++q) { const float h = fminf(__builtin_fmaf((float)acc[ai][0][m][n][q], sgr[q], bgv[n][q]), 7.0f * C2), up = fminf(fmaxf(__builtin_fmaf((float)acc[ai][1][m][n][q], sur[q], buv[n][q]), -7.0f), 7.0f);
;                             const float sg = __builtin_amdgcn_rcpf(1.0f + __builtin_amdgcn_exp2f(-h)); o[4 * n + q] = __builtin_fmaf(up, ACT_SC / C2, ACT_SC / C2) * (h * sg); } }
;                     int w0 = __builtin_amdgcn_cvt_pk_fp8_f32(o[0], o[1], 0, false); w0 = __builtin_amdgcn_cvt_pk_fp8_f32(o[2], o[3], w0, true);
;                     int w1 = __builtin_amdgcn_cvt_pk_fp8_f32(o[4], o[5], 0, false); w1 = __builtin_amdgcn_cvt_pk_fp8_f32(o[6], o[7], w1, true);
;                     wp[hm][0] = (unsigned)w0; wp[hm][1] = (unsigned)w1; }
	v_cvt_f32_i32_e32 v100, v100
	v_cvt_f32_i32_e32 v101, v101
	v_cvt_f32_i32_e32 v102, v102
	v_cvt_f32_i32_e32 v103, v103
	v_pk_mul_f32 v[160:161], v[144:145], v[154:155] op_sel_hi:[1,0]
	v_pk_mul_f32 v[162:163], v[146:147], v[154:155] op_sel_hi:[1,0]
	v_pk_fma_f32 v[96:97], v[96:97], v[160:161], v[136:137]
	v_pk_fma_f32 v[98:99], v[98:99], v[162:163], v[138:139]
	v_pk_mul_f32 v[160:161], v[148:149], v[154:155] op_sel_hi:[1,0]
	v_pk_mul_f32 v[162:163], v[150:151], v[154:155] op_sel_hi:[1,0]
	v_min_f32_e32 v96, 0x41898193, v96
	v_min_f32_e32 v97, 0x41898193, v97
	v_min_f32_e32 v98, 0x41898193, v98
	v_min_f32_e32 v99, 0x41898193, v99
	v_pk_fma_f32 v[100:101], v[100:101], v[160:161], v[140:141]
	v_pk_fma_f32 v[102:103], v[102:103], v[162:163], v[142:143]
	v_exp_f32_e64 v160, -v96
	v_exp_f32_e64 v161, -v97
	v_exp_f32_e64 v162, -v98
	v_exp_f32_e64 v163, -v99
	v_med3_f32 v100, v100, s8, v199
	v_med3_f32 v101, v101, s8, v199
	v_med3_f32 v102, v102, s8, v199
	v_med3_f32 v103, v103, s8, v199
	v_pk_add_f32 v[160:161], v[160:161], 1.0 op_sel_hi:[1,0]
	v_pk_add_f32 v[162:163], v[162:163], 1.0 op_sel_hi:[1,0]
	v_pk_fma_f32 v[100:101], v[100:101], s[100:101], s[100:101]
	v_pk_fma_f32 v[102:103], v[102:103], s[100:101], s[100:101]
	v_rcp_f32_e32 v160, v160
	v_rcp_f32_e32 v161, v161
	v_rcp_f32_e32 v162, v162
	v_rcp_f32_e32 v163, v163
	v_nop
	v_pk_mul_f32 v[96:97], v[96:97], v[160:161]
	v_pk_mul_f32 v[98:99], v[98:99], v[162:163]
	v_pk_mul_f32 v[96:97], v[100:101], v[96:97]
	v_pk_mul_f32 v[98:99], v[102:103], v[98:99]
	v_cvt_pk_fp8_f32 v96, v96, v97
	v_cvt_pk_fp8_f32 v96, v98, v99 op_sel:[0,0,1]
	v_cvt_f32_i32_e32 v80, v80
	v_cvt_f32_i32_e32 v81, v81
	v_cvt_f32_i32_e32 v82, v82
	v_cvt_f32_i32_e32 v83, v83
	v_cvt_f32_i32_e32 v84, v84
	v_cvt_f32_i32_e32 v85, v85
	v_cvt_f32_i32_e32 v86, v86
	v_cvt_f32_i32_e32 v87, v87
	v_pk_mul_f32 v[202:203], v[144:145], v[154:155] op_sel:[0,1] op_sel_hi:[1,1]
	v_pk_mul_f32 v[204:205], v[146:147], v[154:155] op_sel:[0,1] op_sel_hi:[1,1]
	v_pk_fma_f32 v[80:81], v[80:81], v[202:203], v[136:137]
	v_pk_fma_f32 v[82:83], v[82:83], v[204:205], v[138:139]
	v_pk_mul_f32 v[202:203], v[148:149], v[154:155] op_sel:[0,1] op_sel_hi:[1,1]
	v_pk_mul_f32 v[204:205], v[150:151], v[154:155] op_sel:[0,1] op_sel_hi:[1,1]
	v_min_f32_e32 v80, 0x41898193, v80
	v_min_f32_e32 v81, 0x41898193, v81
	v_min_f32_e32 v82, 0x41898193, v82
	v_min_f32_e32 v83, 0x41898193, v83
	v_pk_fma_f32 v[84:85], v[84:85], v[202:203], v[140:141]
	v_pk_fma_f32 v[86:87], v[86:87], v[204:205], v[142:143]
	v_exp_f32_e64 v202, -v80
	v_exp_f32_e64 v203, -v81
	v_exp_f32_e64 v204, -v82
	v_exp_f32_e64 v205, -v83
	v_med3_f32 v84, v84, s8, v199
	v_med3_f32 v85, v85, s8, v199
	v_med3_f32 v86, v86, s8, v199
	v_med3_f32 v87, v87, s8, v199
	v_pk_add_f32 v[202:203], v[202:203], 1.0 op_sel_hi:[1,0]
	v_pk_add_f32 v[204:205], v[204:205], 1.0 op_sel_hi:[1,0]
	v_pk_fma_f32 v[84:85], v[84:85], s[100:101], s[100:101]
	v_pk_fma_f32 v[86:87], v[86:87], s[100:101], s[100:101]
	v_rcp_f32_e32 v202, v202
	v_rcp_f32_e32 v203, v203
	v_rcp_f32_e32 v204, v204
	v_rcp_f32_e32 v205, v205
	v_nop
	v_pk_mul_f32 v[80:81], v[80:81], v[202:203]
	v_pk_mul_f32 v[82:83], v[82:83], v[204:205]
	v_pk_mul_f32 v[80:81], v[84:85], v[80:81]
	v_pk_mul_f32 v[82:83], v[86:87], v[82:83]
	v_cvt_pk_fp8_f32 v98, v80, v81
	v_cvt_pk_fp8_f32 v98, v82, v83 op_sel:[0,0,1]
	v_cvt_f32_i32_e32 v64, v64
	v_cvt_f32_i32_e32 v65, v65
	v_cvt_f32_i32_e32 v66, v66
	v_cvt_f32_i32_e32 v67, v67
	v_cvt_f32_i32_e32 v68, v68
	v_cvt_f32_i32_e32 v69, v69
	v_cvt_f32_i32_e32 v70, v70
	v_cvt_f32_i32_e32 v71, v71
	v_pk_mul_f32 v[160:161], v[144:145], v[156:157] op_sel_hi:[1,0]
	v_pk_mul_f32 v[162:163], v[146:147], v[156:157] op_sel_hi:[1,0]
	v_pk_fma_f32 v[64:65], v[64:65], v[160:161], v[136:137]
	v_pk_fma_f32 v[66:67], v[66:67], v[162:163], v[138:139]
	v_pk_mul_f32 v[160:161], v[148:149], v[156:157] op_sel_hi:[1,0]
	v_pk_mul_f32 v[162:163], v[150:151], v[156:157] op_sel_hi:[1,0]
	v_min_f32_e32 v64, 0x41898193, v64
	v_min_f32_e32 v65, 0x41898193, v65
	v_min_f32_e32 v66, 0x41898193, v66
	v_min_f32_e32 v67, 0x41898193, v67
	v_pk_fma_f32 v[68:69], v[68:69], v[160:161], v[140:141]
	v_pk_fma_f32 v[70:71], v[70:71], v[162:163], v[142:143]
	v_exp_f32_e64 v160, -v64
	v_exp_f32_e64 v161, -v65
	v_exp_f32_e64 v162, -v66
	v_exp_f32_e64 v163, -v67
	v_med3_f32 v68, v68, s8, v199
	v_med3_f32 v69, v69, s8, v199
	v_med3_f32 v70, v70, s8, v199
	v_med3_f32 v71, v71, s8, v199
	v_pk_add_f32 v[160:161], v[160:161], 1.0 op_sel_hi:[1,0]
	v_pk_add_f32 v[162:163], v[162:163], 1.0 op_sel_hi:[1,0]
	v_pk_fma_f32 v[68:69], v[68:69], s[100:101], s[100:101]
	v_pk_fma_f32 v[70:71], v[70:71], s[100:101], s[100:101]
	v_rcp_f32_e32 v160, v160
	v_rcp_f32_e32 v161, v161
	v_rcp_f32_e32 v162, v162
	v_rcp_f32_e32 v163, v163
	v_nop
	v_pk_mul_f32 v[64:65], v[64:65], v[160:161]
	v_pk_mul_f32 v[66:67], v[66:67], v[162:163]
	v_pk_mul_f32 v[64:65], v[68:69], v[64:65]
	v_pk_mul_f32 v[66:67], v[70:71], v[66:67]
	v_cvt_pk_fp8_f32 v64, v64, v65
	v_cvt_pk_fp8_f32 v64, v66, v67 op_sel:[0,0,1]
	v_cvt_f32_i32_e32 v44, v44
	v_cvt_f32_i32_e32 v45, v45
	v_cvt_f32_i32_e32 v46, v46
	v_cvt_f32_i32_e32 v47, v47
	v_cvt_f32_i32_e32 v48, v48
	v_cvt_f32_i32_e32 v49, v49
	v_cvt_f32_i32_e32 v50, v50
	v_cvt_f32_i32_e32 v51, v51
	v_pk_mul_f32 v[202:203], v[144:145], v[156:157] op_sel:[0,1] op_sel_hi:[1,1]
	v_pk_mul_f32 v[204:205], v[146:147], v[156:157] op_sel:[0,1] op_sel_hi:[1,1]
	v_pk_fma_f32 v[44:45], v[44:45], v[202:203], v[136:137]
	v_pk_fma_f32 v[46:47], v[46:47], v[204:205], v[138:139]
	v_pk_mul_f32 v[202:203], v[148:149], v[156:157] op_sel:[0,1] op_sel_hi:[1,1]
	v_pk_mul_f32 v[204:205], v[150:151], v[156:157] op_sel:[0,1] op_sel_hi:[1,1]
; #define PG8_LAS __attribute__((address_space(3)))
;     __device__ __forceinline__ void operator()(const i32x4 (&acc)[2][2][4][2], const Unit& u, int wr, int wc, int fr, int fq, PG8_LAS unsigned* scr) const {
;     ...
;         for (int n = 0; n < 2; ++n) { bgv[n] = *(const PG8_LAS f32x4*)(scr + 512 + cl + 4 * n) * C2; buv[n] = *(const PG8_LAS f32x4*)(scr + 512 + 128 + cl + 4 * n);
;             csg[n] = *(const PG8_LAS f32x4*)(scr + 256 + cl + 4 * n) * (C2 / 127.0f); csu[n] = *(const PG8_LAS f32x4*)(scr + 256 + 128 + cl + 4 * n) * (1.0f / 127.0f); }
; #pragma unroll
;         for (int ai = 0; ai < 2; ++ai)
; #pragma unroll
;             for (int mp = 0; mp < 4; mp += 2) { unsigned wp[2][2];
; #pragma unroll
;                 for (int hm = 0; hm < 2; ++hm) { const int m = mp + hm; const int r = ai * HALF + wr * 64 + m * 16 + fr; const float rs = __uint_as_float(scr[r]); float o[8];
; #pragma unroll
;                     for (int n = 0; n < 2; ++n) { const f32x4 sgr = csg[n] * rs, sur = csu[n] * rs;
; #pragma unroll
;                         for (int q = 0; q < 4; ++q) { const float h = fminf(__builtin_fmaf((float)acc[ai][0][m][n][q], sgr[q], bgv[n][q]), 7.0f * C2), up = fminf(fmaxf(__builtin_fmaf((float)acc[ai][1][m][n][q], sur[q], buv[n][q]), -7.0f), 7.0f);
;                             const float sg = __builtin_amdgcn_rcpf(1.0f + __builtin_amdgcn_exp2f(-h)); o[4 * n + q] = __builtin_fmaf(up, ACT_SC / C2, ACT_SC / C2) * (h * sg); } }
;                     int w0 = __builtin_amdgcn_cvt_pk_fp8_f32(o[0], o[1], 0, false); w0 = __builtin_amdgcn_cvt_pk_fp8_f32(o[2], o[3], w0, true);
;                     int w1 = __builtin_amdgcn_cvt_pk_fp8_f32(o[4], o[5], 0, false); w1 = __builtin_amdgcn_cvt_pk_fp8_f32(o[6], o[7], w1, true);
;                     wp[hm][0] = (unsigned)w0; wp[hm][1] = (unsigned)w1; }
	v_min_f32_e32 v44, 0x41898193, v44
	v_min_f32_e32 v45, 0x41898193, v45
	v_min_f32_e32 v46, 0x41898193, v46
	v_min_f32_e32 v47, 0x41898193, v47
	v_pk_fma_f32 v[48:49], v[48:49], v[202:203], v[140:141]
	v_pk_fma_f32 v[50:51], v[50:51], v[204:205], v[142:143]
	v_exp_f32_e64 v202, -v44
	v_exp_f32_e64 v203, -v45
	v_exp_f32_e64 v204, -v46
	v_exp_f32_e64 v205, -v47
	v_med3_f32 v48, v48, s8, v199
	v_med3_f32 v49, v49, s8, v199
	v_med3_f32 v50, v50, s8, v199
	v_med3_f32 v51, v51, s8, v199
	v_pk_add_f32 v[202:203], v[202:203], 1.0 op_sel_hi:[1,0]
	v_pk_add_f32 v[204:205], v[204:205], 1.0 op_sel_hi:[1,0]
	v_pk_fma_f32 v[48:49], v[48:49], s[100:101], s[100:101]
	v_pk_fma_f32 v[50:51], v[50:51], s[100:101], s[100:101]
	v_rcp_f32_e32 v202, v202
	v_rcp_f32_e32 v203, v203
	v_rcp_f32_e32 v204, v204
	v_rcp_f32_e32 v205, v205
	v_nop
	v_pk_mul_f32 v[44:45], v[44:45], v[202:203]
	v_pk_mul_f32 v[46:47], v[46:47], v[204:205]
	v_pk_mul_f32 v[44:45], v[48:49], v[44:45]
	v_pk_mul_f32 v[46:47], v[50:51], v[46:47]
	v_cvt_pk_fp8_f32 v66, v44, v45
	v_cvt_pk_fp8_f32 v66, v46, v47 op_sel:[0,0,1]
	v_cvt_f32_i32_e32 v24, v24
	v_cvt_f32_i32_e32 v25, v25
	v_cvt_f32_i32_e32 v26, v26
	v_cvt_f32_i32_e32 v27, v27
	v_cvt_f32_i32_e32 v28, v28
	v_cvt_f32_i32_e32 v29, v29
	v_cvt_f32_i32_e32 v30, v30
	v_cvt_f32_i32_e32 v31, v31
	v_pk_mul_f32 v[160:161], v[144:145], v[158:159] op_sel_hi:[1,0]
	v_pk_mul_f32 v[162:163], v[146:147], v[158:159] op_sel_hi:[1,0]
	v_pk_fma_f32 v[24:25], v[24:25], v[160:161], v[136:137]
	v_pk_fma_f32 v[26:27], v[26:27], v[162:163], v[138:139]
	v_pk_mul_f32 v[160:161], v[148:149], v[158:159] op_sel_hi:[1,0]
	v_pk_mul_f32 v[162:163], v[150:151], v[158:159] op_sel_hi:[1,0]
	v_min_f32_e32 v24, 0x41898193, v24
	v_min_f32_e32 v25, 0x41898193, v25
	v_min_f32_e32 v26, 0x41898193, v26
	v_min_f32_e32 v27, 0x41898193, v27
	v_pk_fma_f32 v[28:29], v[28:29], v[160:161], v[140:141]
	v_pk_fma_f32 v[30:31], v[30:31], v[162:163], v[142:143]
	v_exp_f32_e64 v160, -v24
	v_exp_f32_e64 v161, -v25
	v_exp_f32_e64 v162, -v26
	v_exp_f32_e64 v163, -v27
	v_med3_f32 v28, v28, s8, v199
	v_med3_f32 v29, v29, s8, v199
	v_med3_f32 v30, v30, s8, v199
	v_med3_f32 v31, v31, s8, v199
	v_pk_add_f32 v[160:161], v[160:161], 1.0 op_sel_hi:[1,0]
	v_pk_add_f32 v[162:163], v[162:163], 1.0 op_sel_hi:[1,0]
	v_pk_fma_f32 v[28:29], v[28:29], s[100:101], s[100:101]
	v_pk_fma_f32 v[30:31], v[30:31], s[100:101], s[100:101]
	v_rcp_f32_e32 v160, v160
	v_rcp_f32_e32 v161, v161
	v_rcp_f32_e32 v162, v162
	v_rcp_f32_e32 v163, v163
	v_nop
	v_pk_mul_f32 v[24:25], v[24:25], v[160:161]
	v_pk_mul_f32 v[26:27], v[26:27], v[162:163]
	v_pk_mul_f32 v[24:25], v[28:29], v[24:25]
	v_pk_mul_f32 v[26:27], v[30:31], v[26:27]
	v_cvt_pk_fp8_f32 v24, v24, v25
	v_cvt_pk_fp8_f32 v24, v26, v27 op_sel:[0,0,1]
	v_cvt_f32_i32_e32 v8, v8
	v_cvt_f32_i32_e32 v9, v9
	v_cvt_f32_i32_e32 v10, v10
	v_cvt_f32_i32_e32 v11, v11
	v_cvt_f32_i32_e32 v12, v12
	v_cvt_f32_i32_e32 v13, v13
	v_cvt_f32_i32_e32 v14, v14
	v_cvt_f32_i32_e32 v15, v15
	v_pk_mul_f32 v[202:203], v[144:145], v[158:159] op_sel:[0,1] op_sel_hi:[1,1]
	v_pk_mul_f32 v[204:205], v[146:147], v[158:159] op_sel:[0,1] op_sel_hi:[1,1]
	v_pk_fma_f32 v[8:9], v[8:9], v[202:203], v[136:137]
	v_pk_fma_f32 v[10:11], v[10:11], v[204:205], v[138:139]
	v_pk_mul_f32 v[202:203], v[148:149], v[158:159] op_sel:[0,1] op_sel_hi:[1,1]
	v_pk_mul_f32 v[204:205], v[150:151], v[158:159] op_sel:[0,1] op_sel_hi:[1,1]
	v_min_f32_e32 v8, 0x41898193, v8
	v_min_f32_e32 v9, 0x41898193, v9
	v_min_f32_e32 v10, 0x41898193, v10
	v_min_f32_e32 v11, 0x41898193, v11
	v_pk_fma_f32 v[12:13], v[12:13], v[202:203], v[140:141]
	v_pk_fma_f32 v[14:15], v[14:15], v[204:205], v[142:143]
	v_exp_f32_e64 v202, -v8
	v_exp_f32_e64 v203, -v9
	v_exp_f32_e64 v204, -v10
	v_exp_f32_e64 v205, -v11
	v_med3_f32 v12, v12, s8, v199
	v_med3_f32 v13, v13, s8, v199
	v_med3_f32 v14, v14, s8, v199
	v_med3_f32 v15, v15, s8, v199
	v_pk_add_f32 v[202:203], v[202:203], 1.0 op_sel_hi:[1,0]
	v_pk_add_f32 v[204:205], v[204:205], 1.0 op_sel_hi:[1,0]
	v_pk_fma_f32 v[12:13], v[12:13], s[100:101], s[100:101]
	v_pk_fma_f32 v[14:15], v[14:15], s[100:101], s[100:101]
	v_rcp_f32_e32 v202, v202
	v_rcp_f32_e32 v203, v203
	v_rcp_f32_e32 v204, v204
	v_rcp_f32_e32 v205, v205
	v_nop
	v_pk_mul_f32 v[8:9], v[8:9], v[202:203]
	v_pk_mul_f32 v[10:11], v[10:11], v[204:205]
	v_pk_mul_f32 v[8:9], v[12:13], v[8:9]
	v_pk_mul_f32 v[10:11], v[14:15], v[10:11]
	v_cvt_pk_fp8_f32 v26, v8, v9
	v_cvt_pk_fp8_f32 v26, v10, v11 op_sel:[0,0,1]
	v_add_u32_e32 v160, 0x21110, v208
	ds_read_b128 v[136:139], v160
	v_add_u32_e32 v160, 0x21310, v208
	ds_read_b128 v[140:143], v160
	v_add_u32_e32 v160, 0x20d10, v208
	ds_read_b128 v[144:147], v160
	v_add_u32_e32 v160, 0x20f10, v208
	ds_read_b128 v[148:151], v160
	s_waitcnt lgkmcnt(0)
; #define GAS __attribute__((address_space(1)))
;     __device__ __forceinline__ void operator()(const i32x4 (&acc)[2][2][4][2], const Unit& u, int wr, int wc, int fr, int fq, PG8_LAS unsigned* scr) const {
;     ...
;                 for (int hm = 0; hm < 2; ++hm) { const int m = mp + hm; const int r = ai * HALF + wr * 64 + m * 16 + fr; const float rs = __uint_as_float(scr[r]); float o[8];
; #pragma unroll
;                     for (int n = 0; n < 2; ++n) { const f32x4 sgr = csg[n] * rs, sur = csu[n] * rs;
; #pragma unroll
;                         for (int q = 0; q < 4; ++q) { const float h = fminf(__builtin_fmaf((float)acc[ai][0][m][n][q], sgr[q], bgv[n][q]), 7.0f * C2), up = fminf(fmaxf(__builtin_fmaf((float)acc[ai][1][m][n][q], sur[q], buv[n][q]), -7.0f), 7.0f);
;                             const float sg = __builtin_amdgcn_rcpf(1.0f + __builtin_amdgcn_exp2f(-h)); o[4 * n + q] = __builtin_fmaf(up, ACT_SC / C2, ACT_SC / C2) * (h * sg); } }
;                     int w0 = __builtin_amdgcn_cvt_pk_fp8_f32(o[0], o[1], 0, false); w0 = __builtin_amdgcn_cvt_pk_fp8_f32(o[2], o[3], w0, true);
;                     int w1 = __builtin_amdgcn_cvt_pk_fp8_f32(o[4], o[5], 0, false); w1 = __builtin_amdgcn_cvt_pk_fp8_f32(o[6], o[7], w1, true);
;                     wp[hm][0] = (unsigned)w0; wp[hm][1] = (unsigned)w1; }
;                 { auto r0 = __builtin_amdgcn_permlane16_swap(wp[0][0], wp[1][0], false, false); wp[0][0] = r0[0]; wp[1][0] = r0[1];
;                   auto r1 = __builtin_amdgcn_permlane16_swap(wp[0][1], wp[1][1], false, false); wp[0][1] = r1[0]; wp[1][1] = r1[1]; }
;                 const int odd = fq & 1;
;                 const size_t arow = (size_t)(row0 + ai * HALF + (mp + odd) * 16);
;                 *(GAS u32x4*)(act + arow * 1024 + (c0 - 8 * odd)) = (u32x4){wp[0][0], wp[0][1], wp[1][0], wp[1][1]};
	v_mul_f32_e32 v136, 0x401d265f, v136
	v_mul_f32_e32 v137, 0x401d265f, v137
	v_mul_f32_e32 v138, 0x401d265f, v138
	v_mul_f32_e32 v139, 0x401d265f, v139
	v_mul_f32_e32 v144, 0x3c9e6325, v144
	v_mul_f32_e32 v145, 0x3c9e6325, v145
	v_mul_f32_e32 v146, 0x3c9e6325, v146
	v_mul_f32_e32 v147, 0x3c9e6325, v147
	v_mul_f32_e32 v148, 0x3c010204, v148
	v_mul_f32_e32 v149, 0x3c010204, v149
	v_mul_f32_e32 v150, 0x3c010204, v150
	v_mul_f32_e32 v151, 0x3c010204, v151
	v_cvt_f32_i32_e32 v120, v120
	v_cvt_f32_i32_e32 v121, v121
	v_cvt_f32_i32_e32 v122, v122
	v_cvt_f32_i32_e32 v123, v123
	v_cvt_f32_i32_e32 v124, v124
	v_cvt_f32_i32_e32 v125, v125
	v_cvt_f32_i32_e32 v126, v126
	v_cvt_f32_i32_e32 v127, v127
	v_pk_mul_f32 v[160:161], v[144:145], v[152:153] op_sel_hi:[1,0]
	v_pk_mul_f32 v[162:163], v[146:147], v[152:153] op_sel_hi:[1,0]
	v_pk_fma_f32 v[120:121], v[120:121], v[160:161], v[136:137]
	v_pk_fma_f32 v[122:123], v[122:123], v[162:163], v[138:139]
	v_pk_mul_f32 v[160:161], v[148:149], v[152:153] op_sel_hi:[1,0]
	v_pk_mul_f32 v[162:163], v[150:151], v[152:153] op_sel_hi:[1,0]
	v_min_f32_e32 v120, 0x41898193, v120
	v_min_f32_e32 v121, 0x41898193, v121
	v_min_f32_e32 v122, 0x41898193, v122
	v_min_f32_e32 v123, 0x41898193, v123
	v_pk_fma_f32 v[124:125], v[124:125], v[160:161], v[140:141]
	v_pk_fma_f32 v[126:127], v[126:127], v[162:163], v[142:143]
	v_exp_f32_e64 v160, -v120
	v_exp_f32_e64 v161, -v121
	v_exp_f32_e64 v162, -v122
	v_exp_f32_e64 v163, -v123
	v_med3_f32 v124, v124, s8, v199
	v_med3_f32 v125, v125, s8, v199
	v_med3_f32 v126, v126, s8, v199
	v_med3_f32 v127, v127, s8, v199
	v_pk_add_f32 v[160:161], v[160:161], 1.0 op_sel_hi:[1,0]
	v_pk_add_f32 v[162:163], v[162:163], 1.0 op_sel_hi:[1,0]
	v_pk_fma_f32 v[124:125], v[124:125], s[100:101], s[100:101]
	v_pk_fma_f32 v[126:127], v[126:127], s[100:101], s[100:101]
	v_rcp_f32_e32 v160, v160
	v_rcp_f32_e32 v161, v161
	v_rcp_f32_e32 v162, v162
	v_rcp_f32_e32 v163, v163
	v_nop
	v_pk_mul_f32 v[120:121], v[120:121], v[160:161]
	v_pk_mul_f32 v[122:123], v[122:123], v[162:163]
	v_pk_mul_f32 v[120:121], v[124:125], v[120:121]
	v_pk_mul_f32 v[122:123], v[126:127], v[122:123]
	v_cvt_pk_fp8_f32 v129, v120, v121
	v_cvt_pk_fp8_f32 v129, v122, v123 op_sel:[0,0,1]
	v_cvt_f32_i32_e32 v104, v104
	v_cvt_f32_i32_e32 v105, v105
	v_cvt_f32_i32_e32 v106, v106
	v_cvt_f32_i32_e32 v107, v107
	v_cvt_f32_i32_e32 v108, v108
	v_cvt_f32_i32_e32 v109, v109
	v_cvt_f32_i32_e32 v110, v110
	v_cvt_f32_i32_e32 v111, v111
	v_pk_mul_f32 v[202:203], v[144:145], v[152:153] op_sel:[0,1] op_sel_hi:[1,1]
	v_pk_mul_f32 v[204:205], v[146:147], v[152:153] op_sel:[0,1] op_sel_hi:[1,1]
	v_pk_fma_f32 v[104:105], v[104:105], v[202:203], v[136:137]
	v_pk_fma_f32 v[106:107], v[106:107], v[204:205], v[138:139]
	v_pk_mul_f32 v[202:203], v[148:149], v[152:153] op_sel:[0,1] op_sel_hi:[1,1]
	v_pk_mul_f32 v[204:205], v[150:151], v[152:153] op_sel:[0,1] op_sel_hi:[1,1]
	v_min_f32_e32 v104, 0x41898193, v104
	v_min_f32_e32 v105, 0x41898193, v105
	v_min_f32_e32 v106, 0x41898193, v106
	v_min_f32_e32 v107, 0x41898193, v107
	v_pk_fma_f32 v[108:109], v[108:109], v[202:203], v[140:141]
	v_pk_fma_f32 v[110:111], v[110:111], v[204:205], v[142:143]
	v_exp_f32_e64 v202, -v104
	v_exp_f32_e64 v203, -v105
	v_exp_f32_e64 v204, -v106
	v_exp_f32_e64 v205, -v107
	v_med3_f32 v108, v108, s8, v199
	v_med3_f32 v109, v109, s8, v199
	v_med3_f32 v110, v110, s8, v199
	v_med3_f32 v111, v111, s8, v199
	v_pk_add_f32 v[202:203], v[202:203], 1.0 op_sel_hi:[1,0]
	v_pk_add_f32 v[204:205], v[204:205], 1.0 op_sel_hi:[1,0]
	v_pk_fma_f32 v[108:109], v[108:109], s[100:101], s[100:101]
	v_pk_fma_f32 v[110:111], v[110:111], s[100:101], s[100:101]
	v_rcp_f32_e32 v202, v202
	v_rcp_f32_e32 v203, v203
	v_rcp_f32_e32 v204, v204
	v_rcp_f32_e32 v205, v205
	v_nop
	v_pk_mul_f32 v[104:105], v[104:105], v[202:203]
	v_pk_mul_f32 v[106:107], v[106:107], v[204:205]
	v_pk_mul_f32 v[104:105], v[108:109], v[104:105]
	v_pk_mul_f32 v[106:107], v[110:111], v[106:107]
	v_cvt_pk_fp8_f32 v131, v104, v105
	v_cvt_pk_fp8_f32 v131, v106, v107 op_sel:[0,0,1]
	s_nop 1
	v_permlane16_swap_b32_e32 v128, v130
	v_permlane16_swap_b32_e32 v129, v131
	v_add_u32_e32 v160, 0, v185
	v_mov_b32_e32 v161, 0
	v_lshlrev_b64 v[160:161], 10, v[160:161]
	v_lshl_add_u64 v[160:161], s[60:61], 0, v[160:161]
	v_lshl_add_u64 v[160:161], v[160:161], 0, v[206:207]
	global_store_dwordx4 v[160:161], v[128:131], off
	v_cvt_f32_i32_e32 v88, v88
	v_cvt_f32_i32_e32 v89, v89
	v_cvt_f32_i32_e32 v90, v90
	v_cvt_f32_i32_e32 v91, v91
	v_cvt_f32_i32_e32 v92, v92
	v_cvt_f32_i32_e32 v93, v93
	v_cvt_f32_i32_e32 v94, v94
	v_cvt_f32_i32_e32 v95, v95
	v_pk_mul_f32 v[160:161], v[144:145], v[154:155] op_sel_hi:[1,0]
	v_pk_mul_f32 v[162:163], v[146:147], v[154:155] op_sel_hi:[1,0]
	v_pk_fma_f32 v[88:89], v[88:89], v[160:161], v[136:137]
	v_pk_fma_f32 v[90:91], v[90:91], v[162:163], v[138:139]
	v_pk_mul_f32 v[160:161], v[148:149], v[154:155] op_sel_hi:[1,0]
	v_pk_mul_f32 v[162:163], v[150:151], v[154:155] op_sel_hi:[1,0]
	v_min_f32_e32 v88, 0x41898193, v88
	v_min_f32_e32 v89, 0x41898193, v89
	v_min_f32_e32 v90, 0x41898193, v90
	v_min_f32_e32 v91, 0x41898193, v91
	v_pk_fma_f32 v[92:93], v[92:93], v[160:161], v[140:141]
	v_pk_fma_f32 v[94:95], v[94:95], v[162:163], v[142:143]
	v_exp_f32_e64 v160, -v88
	v_exp_f32_e64 v161, -v89
	v_exp_f32_e64 v162, -v90
	v_exp_f32_e64 v163, -v91
	v_med3_f32 v92, v92, s8, v199
	v_med3_f32 v93, v93, s8, v199
	v_med3_f32 v94, v94, s8, v199
	v_med3_f32 v95, v95, s8, v199
	v_pk_add_f32 v[160:161], v[160:161], 1.0 op_sel_hi:[1,0]
	v_pk_add_f32 v[162:163], v[162:163], 1.0 op_sel_hi:[1,0]
	v_pk_fma_f32 v[92:93], v[92:93], s[100:101], s[100:101]
; #define GAS __attribute__((address_space(1)))
;     __device__ __forceinline__ void operator()(const i32x4 (&acc)[2][2][4][2], const Unit& u, int wr, int wc, int fr, int fq, PG8_LAS unsigned* scr) const {
;     ...
;                 for (int hm = 0; hm < 2; ++hm) { const int m = mp + hm; const int r = ai * HALF + wr * 64 + m * 16 + fr; const float rs = __uint_as_float(scr[r]); float o[8];
; #pragma unroll
;                     for (int n = 0; n < 2; ++n) { const f32x4 sgr = csg[n] * rs, sur = csu[n] * rs;
; #pragma unroll
;                         for (int q = 0; q < 4; ++q) { const float h = fminf(__builtin_fmaf((float)acc[ai][0][m][n][q], sgr[q], bgv[n][q]), 7.0f * C2), up = fminf(fmaxf(__builtin_fmaf((float)acc[ai][1][m][n][q], sur[q], buv[n][q]), -7.0f), 7.0f);
;                             const float sg = __builtin_amdgcn_rcpf(1.0f + __builtin_amdgcn_exp2f(-h)); o[4 * n + q] = __builtin_fmaf(up, ACT_SC / C2, ACT_SC / C2) * (h * sg); } }
;                     int w0 = __builtin_amdgcn_cvt_pk_fp8_f32(o[0], o[1], 0, false); w0 = __builtin_amdgcn_cvt_pk_fp8_f32(o[2], o[3], w0, true);
;                     int w1 = __builtin_amdgcn_cvt_pk_fp8_f32(o[4], o[5], 0, false); w1 = __builtin_amdgcn_cvt_pk_fp8_f32(o[6], o[7], w1, true);
;                     wp[hm][0] = (unsigned)w0; wp[hm][1] = (unsigned)w1; }
;                 { auto r0 = __builtin_amdgcn_permlane16_swap(wp[0][0], wp[1][0], false, false); wp[0][0] = r0[0]; wp[1][0] = r0[1];
;                   auto r1 = __builtin_amdgcn_permlane16_swap(wp[0][1], wp[1][1], false, false); wp[0][1] = r1[0]; wp[1][1] = r1[1]; }
;                 const int odd = fq & 1;
;                 const size_t arow = (size_t)(row0 + ai * HALF + (mp + odd) * 16);
;                 *(GAS u32x4*)(act + arow * 1024 + (c0 - 8 * odd)) = (u32x4){wp[0][0], wp[0][1], wp[1][0], wp[1][1]};
	v_pk_fma_f32 v[94:95], v[94:95], s[100:101], s[100:101]
	v_rcp_f32_e32 v160, v160
	v_rcp_f32_e32 v161, v161
	v_rcp_f32_e32 v162, v162
	v_rcp_f32_e32 v163, v163
	v_nop
	v_pk_mul_f32 v[88:89], v[88:89], v[160:161]
	v_pk_mul_f32 v[90:91], v[90:91], v[162:163]
	v_pk_mul_f32 v[88:89], v[92:93], v[88:89]
	v_pk_mul_f32 v[90:91], v[94:95], v[90:91]
	v_cvt_pk_fp8_f32 v97, v88, v89
	v_cvt_pk_fp8_f32 v97, v90, v91 op_sel:[0,0,1]
	v_cvt_f32_i32_e32 v72, v72
	v_cvt_f32_i32_e32 v73, v73
	v_cvt_f32_i32_e32 v74, v74
	v_cvt_f32_i32_e32 v75, v75
	v_cvt_f32_i32_e32 v76, v76
	v_cvt_f32_i32_e32 v77, v77
	v_cvt_f32_i32_e32 v78, v78
	v_cvt_f32_i32_e32 v79, v79
	v_pk_mul_f32 v[202:203], v[144:145], v[154:155] op_sel:[0,1] op_sel_hi:[1,1]
	v_pk_mul_f32 v[204:205], v[146:147], v[154:155] op_sel:[0,1] op_sel_hi:[1,1]
	v_pk_fma_f32 v[72:73], v[72:73], v[202:203], v[136:137]
	v_pk_fma_f32 v[74:75], v[74:75], v[204:205], v[138:139]
	v_pk_mul_f32 v[202:203], v[148:149], v[154:155] op_sel:[0,1] op_sel_hi:[1,1]
	v_pk_mul_f32 v[204:205], v[150:151], v[154:155] op_sel:[0,1] op_sel_hi:[1,1]
	v_min_f32_e32 v72, 0x41898193, v72
	v_min_f32_e32 v73, 0x41898193, v73
	v_min_f32_e32 v74, 0x41898193, v74
	v_min_f32_e32 v75, 0x41898193, v75
	v_pk_fma_f32 v[76:77], v[76:77], v[202:203], v[140:141]
	v_pk_fma_f32 v[78:79], v[78:79], v[204:205], v[142:143]
	v_exp_f32_e64 v202, -v72
	v_exp_f32_e64 v203, -v73
	v_exp_f32_e64 v204, -v74
	v_exp_f32_e64 v205, -v75
	v_med3_f32 v76, v76, s8, v199
	v_med3_f32 v77, v77, s8, v199
	v_med3_f32 v78, v78, s8, v199
	v_med3_f32 v79, v79, s8, v199
	v_pk_add_f32 v[202:203], v[202:203], 1.0 op_sel_hi:[1,0]
	v_pk_add_f32 v[204:205], v[204:205], 1.0 op_sel_hi:[1,0]
	v_pk_fma_f32 v[76:77], v[76:77], s[100:101], s[100:101]
	v_pk_fma_f32 v[78:79], v[78:79], s[100:101], s[100:101]
	v_rcp_f32_e32 v202, v202
	v_rcp_f32_e32 v203, v203
	v_rcp_f32_e32 v204, v204
	v_rcp_f32_e32 v205, v205
	v_nop
	v_pk_mul_f32 v[72:73], v[72:73], v[202:203]
	v_pk_mul_f32 v[74:75], v[74:75], v[204:205]
	v_pk_mul_f32 v[72:73], v[76:77], v[72:73]
	v_pk_mul_f32 v[74:75], v[78:79], v[74:75]
	v_cvt_pk_fp8_f32 v99, v72, v73
	v_cvt_pk_fp8_f32 v99, v74, v75 op_sel:[0,0,1]
	s_nop 1
	v_permlane16_swap_b32_e32 v96, v98
	v_permlane16_swap_b32_e32 v97, v99
	v_add_u32_e32 v160, 32, v185
	v_mov_b32_e32 v161, 0
	v_lshlrev_b64 v[160:161], 10, v[160:161]
	v_lshl_add_u64 v[160:161], s[60:61], 0, v[160:161]
	v_lshl_add_u64 v[160:161], v[160:161], 0, v[206:207]
	global_store_dwordx4 v[160:161], v[96:99], off
	v_cvt_f32_i32_e32 v56, v56
	v_cvt_f32_i32_e32 v57, v57
	v_cvt_f32_i32_e32 v58, v58
	v_cvt_f32_i32_e32 v59, v59
	v_cvt_f32_i32_e32 v60, v60
	v_cvt_f32_i32_e32 v61, v61
	v_cvt_f32_i32_e32 v62, v62
	v_cvt_f32_i32_e32 v63, v63
	v_pk_mul_f32 v[160:161], v[144:145], v[156:157] op_sel_hi:[1,0]
	v_pk_mul_f32 v[162:163], v[146:147], v[156:157] op_sel_hi:[1,0]
	v_pk_fma_f32 v[56:57], v[56:57], v[160:161], v[136:137]
	v_pk_fma_f32 v[58:59], v[58:59], v[162:163], v[138:139]
	v_pk_mul_f32 v[160:161], v[148:149], v[156:157] op_sel_hi:[1,0]
	v_pk_mul_f32 v[162:163], v[150:151], v[156:157] op_sel_hi:[1,0]
	v_min_f32_e32 v56, 0x41898193, v56
	v_min_f32_e32 v57, 0x41898193, v57
	v_min_f32_e32 v58, 0x41898193, v58
	v_min_f32_e32 v59, 0x41898193, v59
	v_pk_fma_f32 v[60:61], v[60:61], v[160:161], v[140:141]
	v_pk_fma_f32 v[62:63], v[62:63], v[162:163], v[142:143]
	v_exp_f32_e64 v160, -v56
	v_exp_f32_e64 v161, -v57
	v_exp_f32_e64 v162, -v58
	v_exp_f32_e64 v163, -v59
	v_med3_f32 v60, v60, s8, v199
	v_med3_f32 v61, v61, s8, v199
	v_med3_f32 v62, v62, s8, v199
	v_med3_f32 v63, v63, s8, v199
	v_pk_add_f32 v[160:161], v[160:161], 1.0 op_sel_hi:[1,0]
	v_pk_add_f32 v[162:163], v[162:163], 1.0 op_sel_hi:[1,0]
	v_pk_fma_f32 v[60:61], v[60:61], s[100:101], s[100:101]
	v_pk_fma_f32 v[62:63], v[62:63], s[100:101], s[100:101]
	v_rcp_f32_e32 v160, v160
	v_rcp_f32_e32 v161, v161
	v_rcp_f32_e32 v162, v162
	v_rcp_f32_e32 v163, v163
	v_nop
	v_pk_mul_f32 v[56:57], v[56:57], v[160:161]
	v_pk_mul_f32 v[58:59], v[58:59], v[162:163]
	v_pk_mul_f32 v[56:57], v[60:61], v[56:57]
	v_pk_mul_f32 v[58:59], v[62:63], v[58:59]
	v_cvt_pk_fp8_f32 v65, v56, v57
	v_cvt_pk_fp8_f32 v65, v58, v59 op_sel:[0,0,1]
	v_cvt_f32_i32_e32 v32, v32
	v_cvt_f32_i32_e32 v33, v33
	v_cvt_f32_i32_e32 v34, v34
	v_cvt_f32_i32_e32 v35, v35
	v_cvt_f32_i32_e32 v36, v36
	v_cvt_f32_i32_e32 v37, v37
	v_cvt_f32_i32_e32 v38, v38
	v_cvt_f32_i32_e32 v39, v39
	v_pk_mul_f32 v[202:203], v[144:145], v[156:157] op_sel:[0,1] op_sel_hi:[1,1]
	v_pk_mul_f32 v[204:205], v[146:147], v[156:157] op_sel:[0,1] op_sel_hi:[1,1]
	v_pk_fma_f32 v[32:33], v[32:33], v[202:203], v[136:137]
	v_pk_fma_f32 v[34:35], v[34:35], v[204:205], v[138:139]
	v_pk_mul_f32 v[202:203], v[148:149], v[156:157] op_sel:[0,1] op_sel_hi:[1,1]
	v_pk_mul_f32 v[204:205], v[150:151], v[156:157] op_sel:[0,1] op_sel_hi:[1,1]
	v_min_f32_e32 v32, 0x41898193, v32
	v_min_f32_e32 v33, 0x41898193, v33
	v_min_f32_e32 v34, 0x41898193, v34
	v_min_f32_e32 v35, 0x41898193, v35
	v_pk_fma_f32 v[36:37], v[36:37], v[202:203], v[140:141]
	v_pk_fma_f32 v[38:39], v[38:39], v[204:205], v[142:143]
	v_exp_f32_e64 v202, -v32
	v_exp_f32_e64 v203, -v33
	v_exp_f32_e64 v204, -v34
	v_exp_f32_e64 v205, -v35
	v_med3_f32 v36, v36, s8, v199
	v_med3_f32 v37, v37, s8, v199
	v_med3_f32 v38, v38, s8, v199
	v_med3_f32 v39, v39, s8, v199
	v_pk_add_f32 v[202:203], v[202:203], 1.0 op_sel_hi:[1,0]
	v_pk_add_f32 v[204:205], v[204:205], 1.0 op_sel_hi:[1,0]
	v_pk_fma_f32 v[36:37], v[36:37], s[100:101], s[100:101]
	v_pk_fma_f32 v[38:39], v[38:39], s[100:101], s[100:101]
	v_rcp_f32_e32 v202, v202
	v_rcp_f32_e32 v203, v203
	v_rcp_f32_e32 v204, v204
	v_rcp_f32_e32 v205, v205
	v_nop
; #define GAS __attribute__((address_space(1)))
;     __device__ __forceinline__ void operator()(const i32x4 (&acc)[2][2][4][2], const Unit& u, int wr, int wc, int fr, int fq, PG8_LAS unsigned* scr) const {
;     ...
;                 for (int hm = 0; hm < 2; ++hm) { const int m = mp + hm; const int r = ai * HALF + wr * 64 + m * 16 + fr; const float rs = __uint_as_float(scr[r]); float o[8];
; #pragma unroll
;                     for (int n = 0; n < 2; ++n) { const f32x4 sgr = csg[n] * rs, sur = csu[n] * rs;
; #pragma unroll
;                         for (int q = 0; q < 4; ++q) { const float h = fminf(__builtin_fmaf((float)acc[ai][0][m][n][q], sgr[q], bgv[n][q]), 7.0f * C2), up = fminf(fmaxf(__builtin_fmaf((float)acc[ai][1][m][n][q], sur[q], buv[n][q]), -7.0f), 7.0f);
;                             const float sg = __builtin_amdgcn_rcpf(1.0f + __builtin_amdgcn_exp2f(-h)); o[4 * n + q] = __builtin_fmaf(up, ACT_SC / C2, ACT_SC / C2) * (h * sg); } }
;                     int w0 = __builtin_amdgcn_cvt_pk_fp8_f32(o[0], o[1], 0, false); w0 = __builtin_amdgcn_cvt_pk_fp8_f32(o[2], o[3], w0, true);
;                     int w1 = __builtin_amdgcn_cvt_pk_fp8_f32(o[4], o[5], 0, false); w1 = __builtin_amdgcn_cvt_pk_fp8_f32(o[6], o[7], w1, true);
;                     wp[hm][0] = (unsigned)w0; wp[hm][1] = (unsigned)w1; }
;                 { auto r0 = __builtin_amdgcn_permlane16_swap(wp[0][0], wp[1][0], false, false); wp[0][0] = r0[0]; wp[1][0] = r0[1];
;                   auto r1 = __builtin_amdgcn_permlane16_swap(wp[0][1], wp[1][1], false, false); wp[0][1] = r1[0]; wp[1][1] = r1[1]; }
;                 const int odd = fq & 1;
;                 const size_t arow = (size_t)(row0 + ai * HALF + (mp + odd) * 16);
;                 *(GAS u32x4*)(act + arow * 1024 + (c0 - 8 * odd)) = (u32x4){wp[0][0], wp[0][1], wp[1][0], wp[1][1]};
;                 __builtin_amdgcn_sched_barrier(0); }
; template <class Epi, class Sched, bool GATHER, int MODE>
; __device__ __forceinline__ void gemm_phase(PG8_LAS unsigned char* lds, PG8_LAS unsigned* scr, const Gemm g, const Sched& S, const Epi& E, int tid_in) {
;     ...
;     auto gather_read = [&](const Unit& uu) { u32x4 o; int tz = tid; asm volatile("" : "+v"(tz));
; #pragma unroll
;         for (int i = 0; i < 2; ++i) { int R, C; stage_rc(tz * 16 + i * 8192, R, C);
; #pragma unroll
	v_pk_mul_f32 v[32:33], v[32:33], v[202:203]
	v_pk_mul_f32 v[34:35], v[34:35], v[204:205]
	v_pk_mul_f32 v[32:33], v[36:37], v[32:33]
	v_pk_mul_f32 v[34:35], v[38:39], v[34:35]
	v_cvt_pk_fp8_f32 v67, v32, v33
	v_cvt_pk_fp8_f32 v67, v34, v35 op_sel:[0,0,1]
	s_nop 1
	v_permlane16_swap_b32_e32 v64, v66
	v_permlane16_swap_b32_e32 v65, v67
	v_add_u32_e32 v160, 128, v185
	v_mov_b32_e32 v161, 0
	v_lshlrev_b64 v[160:161], 10, v[160:161]
	v_lshl_add_u64 v[160:161], s[60:61], 0, v[160:161]
	v_lshl_add_u64 v[160:161], v[160:161], 0, v[206:207]
	global_store_dwordx4 v[160:161], v[64:67], off
	v_cvt_f32_i32_e32 v16, v16
	v_cvt_f32_i32_e32 v17, v17
	v_cvt_f32_i32_e32 v18, v18
	v_cvt_f32_i32_e32 v19, v19
	v_cvt_f32_i32_e32 v20, v20
	v_cvt_f32_i32_e32 v21, v21
	v_cvt_f32_i32_e32 v22, v22
	v_cvt_f32_i32_e32 v23, v23
	v_pk_mul_f32 v[160:161], v[144:145], v[158:159] op_sel_hi:[1,0]
	v_pk_mul_f32 v[162:163], v[146:147], v[158:159] op_sel_hi:[1,0]
	v_pk_fma_f32 v[16:17], v[16:17], v[160:161], v[136:137]
	v_pk_fma_f32 v[18:19], v[18:19], v[162:163], v[138:139]
	v_pk_mul_f32 v[160:161], v[148:149], v[158:159] op_sel_hi:[1,0]
	v_pk_mul_f32 v[162:163], v[150:151], v[158:159] op_sel_hi:[1,0]
	v_min_f32_e32 v16, 0x41898193, v16
	v_min_f32_e32 v17, 0x41898193, v17
	v_min_f32_e32 v18, 0x41898193, v18
	v_min_f32_e32 v19, 0x41898193, v19
	v_pk_fma_f32 v[20:21], v[20:21], v[160:161], v[140:141]
	v_pk_fma_f32 v[22:23], v[22:23], v[162:163], v[142:143]
	v_exp_f32_e64 v160, -v16
	v_exp_f32_e64 v161, -v17
	v_exp_f32_e64 v162, -v18
	v_exp_f32_e64 v163, -v19
	v_med3_f32 v20, v20, s8, v199
	v_med3_f32 v21, v21, s8, v199
	v_med3_f32 v22, v22, s8, v199
	v_med3_f32 v23, v23, s8, v199
	v_pk_add_f32 v[160:161], v[160:161], 1.0 op_sel_hi:[1,0]
	v_pk_add_f32 v[162:163], v[162:163], 1.0 op_sel_hi:[1,0]
	v_pk_fma_f32 v[20:21], v[20:21], s[100:101], s[100:101]
	v_pk_fma_f32 v[22:23], v[22:23], s[100:101], s[100:101]
	v_rcp_f32_e32 v160, v160
	v_rcp_f32_e32 v161, v161
	v_rcp_f32_e32 v162, v162
	v_rcp_f32_e32 v163, v163
	v_nop
	v_pk_mul_f32 v[16:17], v[16:17], v[160:161]
	v_pk_mul_f32 v[18:19], v[18:19], v[162:163]
	v_pk_mul_f32 v[16:17], v[20:21], v[16:17]
	v_pk_mul_f32 v[18:19], v[22:23], v[18:19]
	v_cvt_pk_fp8_f32 v25, v16, v17
	v_cvt_pk_fp8_f32 v25, v18, v19 op_sel:[0,0,1]
	v_cvt_f32_i32_e32 v0, v0
	v_cvt_f32_i32_e32 v1, v1
	v_cvt_f32_i32_e32 v2, v2
	v_cvt_f32_i32_e32 v3, v3
	v_cvt_f32_i32_e32 v4, v4
	v_cvt_f32_i32_e32 v5, v5
	v_cvt_f32_i32_e32 v6, v6
	v_cvt_f32_i32_e32 v7, v7
	v_pk_mul_f32 v[202:203], v[144:145], v[158:159] op_sel:[0,1] op_sel_hi:[1,1]
	v_pk_mul_f32 v[204:205], v[146:147], v[158:159] op_sel:[0,1] op_sel_hi:[1,1]
	v_pk_fma_f32 v[0:1], v[0:1], v[202:203], v[136:137]
	v_pk_fma_f32 v[2:3], v[2:3], v[204:205], v[138:139]
	v_pk_mul_f32 v[202:203], v[148:149], v[158:159] op_sel:[0,1] op_sel_hi:[1,1]
	v_pk_mul_f32 v[204:205], v[150:151], v[158:159] op_sel:[0,1] op_sel_hi:[1,1]
	v_min_f32_e32 v0, 0x41898193, v0
	v_min_f32_e32 v1, 0x41898193, v1
	v_min_f32_e32 v2, 0x41898193, v2
	v_min_f32_e32 v3, 0x41898193, v3
	v_pk_fma_f32 v[4:5], v[4:5], v[202:203], v[140:141]
	v_pk_fma_f32 v[6:7], v[6:7], v[204:205], v[142:143]
	v_exp_f32_e64 v202, -v0
	v_exp_f32_e64 v203, -v1
	v_exp_f32_e64 v204, -v2
	v_exp_f32_e64 v205, -v3
	v_med3_f32 v4, v4, s8, v199
	v_med3_f32 v5, v5, s8, v199
	v_med3_f32 v6, v6, s8, v199
	v_med3_f32 v7, v7, s8, v199
	v_pk_add_f32 v[202:203], v[202:203], 1.0 op_sel_hi:[1,0]
	v_pk_add_f32 v[204:205], v[204:205], 1.0 op_sel_hi:[1,0]
	v_pk_fma_f32 v[4:5], v[4:5], s[100:101], s[100:101]
	v_pk_fma_f32 v[6:7], v[6:7], s[100:101], s[100:101]
	v_rcp_f32_e32 v202, v202
	v_rcp_f32_e32 v203, v203
	v_rcp_f32_e32 v204, v204
	v_rcp_f32_e32 v205, v205
	v_nop
	v_pk_mul_f32 v[0:1], v[0:1], v[202:203]
	v_pk_mul_f32 v[2:3], v[2:3], v[204:205]
	v_pk_mul_f32 v[0:1], v[4:5], v[0:1]
	v_pk_mul_f32 v[2:3], v[6:7], v[2:3]
	v_cvt_pk_fp8_f32 v27, v0, v1
	v_cvt_pk_fp8_f32 v27, v2, v3 op_sel:[0,0,1]
	s_nop 1
	v_permlane16_swap_b32_e32 v24, v26
	v_permlane16_swap_b32_e32 v25, v27
	v_add_u32_e32 v160, 160, v185
	v_mov_b32_e32 v161, 0
	v_lshlrev_b64 v[160:161], 10, v[160:161]
	v_lshl_add_u64 v[160:161], s[60:61], 0, v[160:161]
	v_lshl_add_u64 v[160:161], v[160:161], 0, v[206:207]
	global_store_dwordx4 v[160:161], v[24:27], off
	s_cmp_eq_u32 s38, s89
	s_mov_b64 s[10:11], -1
	s_cbranch_scc1 .LBB0_786
	v_mov_b32_e32 v0, v168
	s_andn2_b64 vcc, exec, s[58:59]
	v_ashrrev_i32_e32 v2, 31, v0
	v_lshrrev_b32_e32 v2, 26, v2
	v_lshlrev_b32_e32 v6, 4, v0
	v_lshl_add_u32 v1, v0, 2, 0
	v_add_u32_e32 v2, v0, v2
	v_bfe_i32 v0, v0, 27, 1
	v_lshrrev_b32_e32 v0, 22, v0
	v_add_u32_e32 v0, v6, v0
	v_and_b32_e32 v0, 0xfffffc00, v0
	v_sub_u32_e32 v0, v6, v0
	v_ashrrev_i32_e32 v4, 6, v2
	v_lshrrev_b32_e32 v2, 4, v0
	v_bitop3_b32 v5, v2, v0, 32 bitop3:0x6c
	v_ashrrev_i32_e32 v2, 31, v5
	v_lshrrev_b32_e32 v2, 26, v2
	v_lshlrev_b32_e32 v0, 3, v4
	v_add_u32_e32 v7, v5, v2
	v_and_b32_e32 v0, -16, v0
	v_ashrrev_i32_e32 v2, 6, v7
	v_add3_u32 v8, v0, s23, v2
	v_cmp_gt_i32_e64 s[40:41], s92, v8
	v_add_u32_e32 v8, 0x80, v8
	v_cmp_gt_i32_e64 s[38:39], s92, v8
	v_add_u32_e32 v8, 0x2000, v6
	v_ashrrev_i32_e32 v6, 31, v8
	v_lshrrev_b32_e32 v6, 22, v6
	v_add_u32_e32 v6, v8, v6
	v_ashrrev_i32_e32 v6, 10, v6
	v_mul_i32_i24_e32 v9, 0x400, v6
	v_sub_u32_e32 v8, v8, v9
	v_lshrrev_b32_e32 v9, 4, v8
	v_bitop3_b32 v8, v9, v8, 32 bitop3:0x6c
	v_lshlrev_b32_e32 v9, 3, v6
	v_and_b32_e32 v10, -16, v9
	v_ashrrev_i32_e32 v9, 31, v8
	v_add_u32_e32 v1, 0x21900, v1
	v_lshrrev_b32_e32 v9, 26, v9
	ds_read2st64_b32 v[2:3], v1 offset1:8
	ds_read2st64_b32 v[0:1], v1 offset0:16 offset1:24
	v_add_u32_e32 v9, v8, v9
	v_ashrrev_i32_e32 v11, 6, v9
	v_add3_u32 v10, v10, s23, v11
	v_cmp_gt_i32_e64 s[42:43], s92, v10
	v_add_u32_e32 v10, 0x80, v10
	v_cmp_gt_i32_e64 s[44:45], s92, v10
	s_cbranch_vccnz .LBB0_785
	s_barrier
	s_branch .LBB0_785

; __global__ void __launch_bounds__(NWAVES * 64, 2) fwd_kernel(Args args) {
	.amdhsa_kernel _Z10fwd_kernel4Args
		.amdhsa_group_segment_fixed_size 0
		.amdhsa_private_segment_fixed_size 0
		.amdhsa_kernarg_size 448
		.amdhsa_user_sgpr_count 2
		.amdhsa_user_sgpr_dispatch_ptr 0
		.amdhsa_user_sgpr_queue_ptr 0
		.amdhsa_user_sgpr_kernarg_segment_ptr 1
		.amdhsa_user_sgpr_dispatch_id 0
		.amdhsa_user_sgpr_kernarg_preload_length 0
		.amdhsa_user_sgpr_kernarg_preload_offset 0
		.amdhsa_user_sgpr_private_segment_size 0
		.amdhsa_uses_dynamic_stack 0
		.amdhsa_enable_private_segment 0
		.amdhsa_system_sgpr_workgroup_id_x 1
		.amdhsa_system_sgpr_workgroup_id_y 0
		.amdhsa_system_sgpr_workgroup_id_z 0
		.amdhsa_system_sgpr_workgroup_info 0
		.amdhsa_system_vgpr_workitem_id 0
		.amdhsa_next_free_vgpr 256
		.amdhsa_next_free_sgpr 102
		.amdhsa_accum_offset 256
		.amdhsa_reserve_vcc 1
		.amdhsa_float_round_mode_32 0
		.amdhsa_float_round_mode_16_64 0
		.amdhsa_float_denorm_mode_32 3
		.amdhsa_float_denorm_mode_16_64 3
		.amdhsa_dx10_clamp 1
		.amdhsa_ieee_mode 1
		.amdhsa_fp16_overflow 0
		.amdhsa_tg_split 0
		.amdhsa_exception_fp_ieee_invalid_op 0
		.amdhsa_exception_fp_denorm_src 0
		.amdhsa_exception_fp_ieee_div_zero 0
		.amdhsa_exception_fp_ieee_overflow 0
		.amdhsa_exception_fp_ieee_underflow 0
		.amdhsa_exception_fp_ieee_inexact 0
		.amdhsa_exception_int_div_zero 0
	.end_amdhsa_kernel

; __global__ void __launch_bounds__(NWAVES * 64, 2) fwd_kernel(Args args) {
amdhsa.kernels:
  - .agpr_count:     0
    .args:
      - .offset:         0
        .size:           192
        .value_kind:     by_value
      - .offset:         192
        .size:           4
        .value_kind:     hidden_block_count_x
      - .offset:         196
        .size:           4
        .value_kind:     hidden_block_count_y
      - .offset:         200
        .size:           4
        .value_kind:     hidden_block_count_z
      - .offset:         204
        .size:           2
        .value_kind:     hidden_group_size_x
      - .offset:         206
        .size:           2
        .value_kind:     hidden_group_size_y
      - .offset:         208
        .size:           2
        .value_kind:     hidden_group_size_z
      - .offset:         210
        .size:           2
        .value_kind:     hidden_remainder_x
      - .offset:         212
        .size:           2
        .value_kind:     hidden_remainder_y
      - .offset:         214
        .size:           2
        .value_kind:     hidden_remainder_z
      - .offset:         232
        .size:           8
        .value_kind:     hidden_global_offset_x
      - .offset:         240
        .size:           8
        .value_kind:     hidden_global_offset_y
      - .offset:         248
        .size:           8
        .value_kind:     hidden_global_offset_z
      - .offset:         256
        .size:           2
        .value_kind:     hidden_grid_dims
      - .offset:         312
        .size:           4
        .value_kind:     hidden_dynamic_lds_size
    .group_segment_fixed_size: 0
    .kernarg_segment_align: 8
    .kernarg_segment_size: 448
    .language:       OpenCL C
    .language_version:
      - 2
      - 0
    .max_flat_workgroup_size: 512
    .name:           _Z10fwd_kernel4Args
    .private_segment_fixed_size: 0
    .sgpr_count:     108
    .sgpr_spill_count: 232
    .symbol:         _Z10fwd_kernel4Args.kd
    .uniform_work_group_size: 1
    .uses_dynamic_stack: false
    .vgpr_count:     256
    .vgpr_spill_count: 0
    .wavefront_size: 64
